# speedup vs baseline: 1.1296x; 1.0028x over previous
_Z6conv_kILi512ELi256ELi3ELi64ELi1ELi1ELb0EEvPKDF16_S1_PKfS3_PDF16_S4_S1_fS3_S3_S3_S3_:
	s_lshl_b32 s3, s2, 3
	s_load_dwordx2 s[36:37], s[0:1], 0x0
	s_load_dwordx4 s[4:7], s[0:1], 0x10
	s_load_dwordx2 s[30:31], s[0:1], 0x30
	s_and_b32 s3, s3, 56
	s_ashr_i32 s8, s2, 5
	s_add_i32 s3, s3, s8
	v_readfirstlane_b32 s42, v0
	s_lshl_b32 s8, s3, 2
	s_bfe_u32 s38, s2, 0x20003
	s_and_b32 s33, s8, 56
	s_lshr_b32 s52, s42, 6
	s_ashr_i32 s40, s3, 4
	s_and_b32 s27, s2, 32
	s_lshl_b32 s2, s38, 8
	v_bfe_u32 v29, v0, 3, 3
	v_and_b32_e32 v2, 7, v0
	s_waitcnt lgkmcnt(0)
	s_add_u32 s2, s4, s2
	v_bitop3_b32 v2, v29, v2, 6 bitop3:0x6c
	s_addc_u32 s3, s5, 0
	v_and_b32_e32 v18, 48, v0
	v_mov_b32_e32 v19, 0
	v_lshlrev_b32_e32 v20, 3, v2
	v_lshl_add_u64 v[2:3], s[2:3], 0, v[18:19]
	s_load_dword s26, s[6:7], 0x0
	global_load_dwordx4 v[14:17], v[2:3], off
	v_lshl_add_u64 v[4:5], v[2:3], 0, 64
	s_mov_b64 s[2:3], 0x80
	global_load_dwordx4 v[10:13], v[4:5], off
	v_lshl_add_u64 v[4:5], v[2:3], 0, s[2:3]
	s_mov_b64 s[2:3], 0xc0
	v_lshl_add_u64 v[2:3], v[2:3], 0, s[2:3]
	v_lshl_or_b32 v18, s52, 3, v29
	s_mov_b32 s2, 0x1e1e1e1f
	v_mul_hi_u32 v21, v18, s2
	v_lshrrev_b32_e32 v21, 2, v21
	s_movk_i32 s8, 0xffde
	s_add_i32 s24, s33, -1
	global_load_dwordx4 v[6:9], v[4:5], off
	v_mul_lo_u32 v22, v21, s8
	v_add_u32_e32 v25, s24, v21
	s_add_i32 s25, s27, -1
	s_movk_i32 s9, 0x154
	global_load_dwordx4 v[2:5], v[2:3], off
	v_add3_u32 v24, s25, v18, v22
	v_cmp_gt_u32_e64 s[2:3], s9, v18
	v_cmp_gt_u32_e32 vcc, 64, v25
	s_and_b64 s[6:7], s[2:3], vcc
	v_cmp_gt_u32_e64 s[4:5], 64, v24
	v_and_b32_e32 v1, 63, v0
	s_and_b64 s[10:11], s[6:7], s[4:5]
	v_mov_b64_e32 v[22:23], s[30:31]
	v_lshlrev_b32_e32 v18, 1, v20
	s_and_saveexec_b64 s[6:7], s[10:11]
	s_lshl_b32 s10, s40, 15
	v_lshlrev_b32_e32 v22, 6, v25
	v_or3_b32 v22, v22, s10, v24
	v_ashrrev_i32_e32 v23, 31, v22
	v_lshlrev_b64 v[22:23], 7, v[22:23]
	v_lshl_add_u64 v[22:23], s[36:37], 0, v[22:23]
	v_lshl_add_u64 v[22:23], v[22:23], 0, v[18:19]
	s_or_b64 exec, exec, s[6:7]
	s_lshl_b32 s43, s52, 10
	v_lshlrev_b32_e32 v120, 4, v1
	v_or_b32_e32 v19, s43, v120
	s_add_i32 s13, s52, 8
	v_readfirstlane_b32 s6, v19
	s_mov_b32 m0, s6
	s_mov_b32 s12, 0x3c3c3c3d
	v_mov_b64_e32 v[184:185], v[22:23]
	global_load_lds_dwordx4 v[22:23], off
	v_lshl_or_b32 v22, s13, 3, v29
	v_mul_hi_u32 v19, v22, s12
	v_lshrrev_b32_e32 v25, 3, v19
	v_mul_lo_u32 v23, v25, s8
	v_add_u32_e32 v19, s24, v25
	v_add3_u32 v26, s25, v22, v23
	v_cmp_gt_u32_e64 s[6:7], s9, v22
	v_cmp_gt_u32_e32 vcc, 64, v19
	s_and_b64 s[10:11], s[6:7], vcc
	v_cmp_gt_u32_e64 s[8:9], 64, v26
	s_and_b64 s[14:15], s[10:11], s[8:9]
	v_mov_b64_e32 v[22:23], s[30:31]
	s_and_saveexec_b64 s[10:11], s[14:15]
	s_lshl_b32 s14, s40, 15
	v_lshlrev_b32_e32 v19, 6, v19
	v_or3_b32 v22, v19, s14, v26
	v_ashrrev_i32_e32 v23, 31, v22
	v_lshlrev_b64 v[22:23], 7, v[22:23]
	v_lshl_add_u64 v[22:23], s[36:37], 0, v[22:23]
	v_mov_b32_e32 v19, 0
	v_lshl_add_u64 v[22:23], v[22:23], 0, v[18:19]
	s_or_b64 exec, exec, s[10:11]
	s_lshl_b32 s44, s13, 10
	v_or_b32_e32 v19, s44, v120
	s_add_i32 s18, s52, 16
	v_readfirstlane_b32 s10, v19
	s_mov_b32 m0, s10
	s_movk_i32 s16, 0xffde
	v_mov_b64_e32 v[186:187], v[22:23]
	global_load_lds_dwordx4 v[22:23], off
	v_lshl_or_b32 v22, s18, 3, v29
	v_mul_hi_u32 v19, v22, s12
	v_lshrrev_b32_e32 v27, 3, v19
	v_mul_lo_u32 v23, v27, s16
	v_add_u32_e32 v19, s24, v27
	s_movk_i32 s17, 0x154
	v_add3_u32 v28, s25, v22, v23
	v_cmp_gt_u32_e64 s[10:11], s17, v22
	v_cmp_gt_u32_e32 vcc, 64, v19
	s_and_b64 s[14:15], s[10:11], vcc
	v_cmp_gt_u32_e64 s[12:13], 64, v28
	s_and_b64 s[20:21], s[14:15], s[12:13]
	v_mov_b64_e32 v[22:23], s[30:31]
	s_and_saveexec_b64 s[14:15], s[20:21]
	s_lshl_b32 s19, s40, 15
	v_lshlrev_b32_e32 v19, 6, v19
	v_or3_b32 v22, v19, s19, v28
	v_ashrrev_i32_e32 v23, 31, v22
	v_lshlrev_b64 v[22:23], 7, v[22:23]
	v_lshl_add_u64 v[22:23], s[36:37], 0, v[22:23]
	v_mov_b32_e32 v19, 0
	v_lshl_add_u64 v[22:23], v[22:23], 0, v[18:19]
	s_or_b64 exec, exec, s[14:15]
	s_lshl_b32 s45, s18, 10
	v_or_b32_e32 v19, s45, v120
	s_add_i32 s21, s52, 24
	v_readfirstlane_b32 s14, v19
	s_mov_b32 m0, s14
	s_mov_b32 s20, 0x3c3c3c3d
	v_mov_b64_e32 v[188:189], v[22:23]
	global_load_lds_dwordx4 v[22:23], off
	v_lshl_or_b32 v22, s21, 3, v29
	v_mul_hi_u32 v19, v22, s20
	v_lshrrev_b32_e32 v30, 3, v19
	v_mul_lo_u32 v23, v30, s16
	v_add_u32_e32 v19, s24, v30
	v_add3_u32 v31, s25, v22, v23
	v_cmp_gt_u32_e64 s[14:15], s17, v22
	v_cmp_gt_u32_e32 vcc, 64, v19
	s_and_b64 s[18:19], s[14:15], vcc
	v_cmp_gt_u32_e64 s[16:17], 64, v31
	s_and_b64 s[22:23], s[18:19], s[16:17]
	v_mov_b64_e32 v[22:23], s[30:31]
	s_and_saveexec_b64 s[18:19], s[22:23]
	s_lshl_b32 s22, s40, 15
	v_lshlrev_b32_e32 v19, 6, v19
	v_or3_b32 v22, v19, s22, v31
	v_ashrrev_i32_e32 v23, 31, v22
	v_lshlrev_b64 v[22:23], 7, v[22:23]
	v_lshl_add_u64 v[22:23], s[36:37], 0, v[22:23]
	v_mov_b32_e32 v19, 0
	v_lshl_add_u64 v[22:23], v[22:23], 0, v[18:19]
	s_or_b64 exec, exec, s[18:19]
	s_lshl_b32 s46, s21, 10
	v_or_b32_e32 v19, s46, v120
	s_add_i32 s28, s52, 32
	v_readfirstlane_b32 s18, v19
	s_mov_b32 m0, s18
	s_movk_i32 s18, 0xffde
	v_mov_b64_e32 v[190:191], v[22:23]
	global_load_lds_dwordx4 v[22:23], off
	v_lshl_or_b32 v22, s28, 3, v29
	v_mul_hi_u32 v19, v22, s20
	v_lshrrev_b32_e32 v32, 3, v19
	v_mul_lo_u32 v23, v32, s18
	v_add_u32_e32 v19, s24, v32
	s_movk_i32 s18, 0x154
	v_add3_u32 v33, s25, v22, v23
	v_cmp_gt_u32_e64 s[18:19], s18, v22
	v_cmp_gt_u32_e32 vcc, 64, v19
	s_and_b64 s[22:23], s[18:19], vcc
	v_cmp_gt_u32_e64 s[20:21], 64, v33
	s_and_b64 s[22:23], s[22:23], s[20:21]
	s_xor_b64 s[22:23], s[22:23], -1
	s_and_saveexec_b64 s[34:35], s[22:23]
	s_xor_b64 s[22:23], exec, s[34:35]
	s_lshl_b32 s29, s40, 15
	s_or_saveexec_b64 s[22:23], s[22:23]
	v_mov_b32_e32 v34, s29
	v_mov_b64_e32 v[22:23], s[30:31]
	s_xor_b64 exec, exec, s[22:23]
	s_lshl_b32 s29, s40, 15
	v_lshlrev_b32_e32 v19, 6, v19
	v_or3_b32 v22, v19, s29, v33
	v_ashrrev_i32_e32 v23, 31, v22
	v_lshlrev_b64 v[22:23], 7, v[22:23]
	v_lshl_add_u64 v[22:23], s[36:37], 0, v[22:23]
	v_mov_b32_e32 v19, 0
	v_lshl_add_u64 v[22:23], v[22:23], 0, v[18:19]
	v_mov_b32_e32 v34, s29
	s_or_b64 exec, exec, s[22:23]
	s_lshl_b32 s47, s28, 10
	v_or_b32_e32 v18, s47, v120
	s_add_i32 s39, s52, 40
	v_readfirstlane_b32 s22, v18
	s_mov_b32 m0, s22
	v_lshl_or_b32 v18, s39, 3, v29
	v_mov_b64_e32 v[192:193], v[22:23]
	global_load_lds_dwordx4 v[22:23], off
	s_mov_b32 s22, 0x3c3c3c3d
	v_mul_hi_u32 v19, v18, s22
	v_lshrrev_b32_e32 v22, 3, v19
	s_movk_i32 s22, 0xffde
	s_load_dwordx2 s[34:35], s[0:1], 0x8
	v_mul_lo_u32 v19, v22, s22
	v_add_u32_e32 v35, s24, v22
	s_movk_i32 s22, 0x154
	v_add3_u32 v23, s25, v18, v19
	v_cmp_gt_u32_e64 s[22:23], s22, v18
	v_cmp_gt_u32_e32 vcc, 64, v35
	s_and_b64 s[28:29], s[22:23], vcc
	v_cmp_gt_u32_e64 s[24:25], 64, v23
	s_and_b64 s[28:29], s[28:29], s[24:25]
	s_xor_b64 s[28:29], s[28:29], -1
	s_and_saveexec_b64 s[48:49], s[28:29]
	s_xor_b64 s[28:29], exec, s[48:49]
	s_or_saveexec_b64 s[28:29], s[28:29]
	v_mov_b64_e32 v[18:19], s[30:31]
	s_xor_b64 exec, exec, s[28:29]
	v_lshlrev_b32_e32 v18, 6, v35
	v_or3_b32 v18, v18, v34, v23
	v_ashrrev_i32_e32 v19, 31, v18
	v_lshlrev_b64 v[18:19], 7, v[18:19]
	v_lshl_add_u64 v[18:19], s[36:37], 0, v[18:19]
	v_lshlrev_b32_e32 v36, 1, v20
	v_mov_b32_e32 v37, 0
	v_lshl_add_u64 v[18:19], v[18:19], 0, v[36:37]
	s_or_b64 exec, exec, s[28:29]
	v_lshrrev_b32_e32 v122, 4, v1
	v_bitop3_b32 v35, v122, v0, 6 bitop3:0x78
	s_and_b32 s48, s52, 3
	v_lshl_or_b32 v29, v29, 6, s43
	s_movk_i32 s50, 0xdc0
	v_and_b32_e32 v121, 15, v0
	v_lshlrev_b32_e32 v35, 4, v35
	s_lshr_b32 s49, s42, 8
	v_and_or_b32 v29, v29, s50, v20
	s_mul_i32 s50, s48, 0x44
	v_lshl_or_b32 v35, v121, 7, v35
	v_add_u32_e32 v123, s50, v121
	v_lshl_or_b32 v35, s49, 13, v35
	s_lshl_b32 s50, s39, 10
	s_lshl_b32 s41, s38, 6
	v_add_u32_e32 v125, 0x18000, v35
	v_or_b32_e32 v35, s50, v120
	s_lshl_b32 s38, s38, 13
	v_readfirstlane_b32 s39, v35
	s_waitcnt lgkmcnt(0)
	s_add_u32 s38, s34, s38
	s_mul_hi_u32 s57, s42, 0x38e38e39
	s_mov_b32 m0, s39
	s_addc_u32 s39, s35, 0
	s_lshr_b32 s34, s57, 12
	s_mulk_i32 s34, 0xffc1
	s_add_i32 s34, s34, s49
	s_lshl_b32 s56, s52, 11
	s_ashr_i32 s35, s34, 31
	s_add_i32 s52, s56, 0x18000
	s_lshl_b64 s[34:35], s[34:35], 15
	s_add_u32 s34, s38, s34
	s_addc_u32 s35, s39, s35
	s_add_i32 s54, s49, 2
	s_mul_hi_u32 s55, s54, 0x38e38e4
	s_mulk_i32 s55, 0xffc1
	s_add_i32 s54, s55, s54
	v_mov_b64_e32 v[194:195], v[18:19]
	global_load_lds_dwordx4 v[18:19], off
	v_lshlrev_b32_e32 v18, 1, v29
	v_mov_b32_e32 v19, 0
	s_mov_b32 m0, s52
	s_ashr_i32 s55, s54, 31
	v_lshl_add_u64 v[36:37], s[34:35], 0, v[18:19]
	global_load_lds_dwordx4 v18, s[34:35]
	s_mov_b64 s[34:35], 0x400
	s_add_i32 m0, s56, 0x18400
	s_lshl_b64 s[54:55], s[54:55], 15
	v_lshl_add_u64 v[36:37], v[36:37], 0, s[34:35]
	s_add_u32 s54, s38, s54
	global_load_lds_dwordx4 v[36:37], off
	s_addc_u32 s55, s39, s55
	s_add_i32 m0, s56, 0x1c000
	v_lshl_add_u64 v[36:37], s[54:55], 0, v[18:19]
	global_load_lds_dwordx4 v18, s[54:55]
	s_add_i32 s54, s49, 4
	s_mul_hi_u32 s55, s54, 0x38e38e4
	s_mulk_i32 s55, 0xffc1
	s_add_i32 s54, s55, s54
	s_ashr_i32 s55, s54, 31
	s_add_i32 m0, s56, 0x1c400
	s_lshl_b64 s[54:55], s[54:55], 15
	s_add_u32 s54, s38, s54
	v_lshl_add_u64 v[36:37], v[36:37], 0, s[34:35]
	s_addc_u32 s55, s39, s55
	global_load_lds_dwordx4 v[36:37], off
	s_add_i32 m0, s56, 0x20000
	v_lshl_add_u64 v[36:37], s[54:55], 0, v[18:19]
	global_load_lds_dwordx4 v18, s[54:55]
	v_lshl_add_u64 v[36:37], v[36:37], 0, s[34:35]
	s_add_i32 m0, s56, 0x20400
	s_lshr_b32 s54, s57, 9
	global_load_lds_dwordx4 v[36:37], off
	s_mul_i32 s54, s54, -9
	s_add_i32 s54, s54, s49
	s_mul_hi_i32 s55, s54, 0x55555556
	s_lshr_b32 s56, s55, 31
	s_add_i32 s55, s55, s56
	s_mul_i32 s55, s55, 31
	s_add_i32 s55, s55, s54
	s_bitcmp1_b32 s57, 9
	s_waitcnt vmcnt(4) lgkmcnt(0)
	s_barrier
	s_cselect_b32 s54, 0xc000, 0
	ds_read_b128 v[62:65], v125
	v_add_u32_e32 v29, s55, v123
	v_add_u32_e32 v124, 34, v123
	ds_read_b128 v[58:61], v125 offset:2048
	v_bitop3_b32 v35, v29, v122, 6 bitop3:0x6c
	v_lshl_add_u32 v29, v29, 7, s54
	v_lshl_or_b32 v139, v35, 4, v29
	ds_read_b128 v[70:73], v139
	v_add_u32_e32 v29, s55, v124
	ds_read_b128 v[66:69], v139 offset:2048
	v_bitop3_b32 v35, v29, v122, 6 bitop3:0x6c
	v_lshl_add_u32 v29, v29, 7, s54
	v_lshl_or_b32 v140, v35, 4, v29
	ds_read_b128 v[82:85], v140
	s_load_dwordx2 s[28:29], s[0:1], 0x20
	ds_read_b128 v[78:81], v140 offset:2048
	ds_read_b128 v[90:93], v125 offset:4096
	ds_read_b128 v[86:89], v125 offset:6144
	v_add_u32_e32 v127, s33, v21
	v_lshlrev_b32_e32 v20, 1, v20
	v_mov_b32_e32 v21, v19
	v_xor_b32_e32 v126, 64, v125
	s_mov_b32 s51, 0
	s_mov_b32 s53, 1
	v_add_u32_e32 v128, v34, v24
	v_lshl_add_u64 v[114:115], s[36:37], 0, v[20:21]
	v_add_u32_e32 v129, s33, v25
	v_add_u32_e32 v130, v34, v26
	v_add_u32_e32 v131, s33, v27
	v_add_u32_e32 v132, v34, v28
	v_add_u32_e32 v133, s33, v30
	v_add_u32_e32 v134, v34, v31
	v_add_u32_e32 v135, s33, v32
	v_add_u32_e32 v136, v34, v33
	v_add_u32_e32 v137, s33, v22
	v_add_u32_e32 v138, v34, v23
	v_lshl_add_u64 v[116:117], s[38:39], 0, v[18:19]
	s_mov_b64 s[36:37], 0
	s_mov_b32 s38, 0
	s_mov_b32 s39, 0
	v_mov_b32_e32 v18, v19
	v_mov_b32_e32 v20, v19
	v_mov_b32_e32 v22, v19
	v_mov_b32_e32 v23, v19
	v_mov_b32_e32 v24, v19
	v_mov_b32_e32 v25, v19
	v_mov_b32_e32 v26, v19
	v_mov_b32_e32 v27, v19
	v_mov_b32_e32 v28, v19
	v_mov_b32_e32 v29, v19
	v_mov_b32_e32 v42, v19
	v_mov_b32_e32 v43, v19
	v_mov_b32_e32 v44, v19
	v_mov_b32_e32 v45, v19
	v_mov_b32_e32 v50, v19
	v_mov_b32_e32 v51, v19
	v_mov_b32_e32 v52, v19
	v_mov_b32_e32 v53, v19
	v_mov_b32_e32 v54, v19
	v_mov_b32_e32 v55, v19
	v_mov_b32_e32 v56, v19
	v_mov_b32_e32 v57, v19
	v_mov_b32_e32 v74, v19
	v_mov_b32_e32 v75, v19
	v_mov_b32_e32 v76, v19
	v_mov_b32_e32 v77, v19
	v_mov_b32_e32 v94, v19
	v_mov_b32_e32 v95, v19
	v_mov_b32_e32 v96, v19
	v_mov_b32_e32 v97, v19
	v_mov_b32_e32 v98, v19
	v_mov_b32_e32 v99, v19
	v_mov_b32_e32 v100, v19
	v_mov_b32_e32 v101, v19
	v_mov_b32_e32 v102, v19
	v_mov_b32_e32 v103, v19
	v_mov_b32_e32 v104, v19
	v_mov_b32_e32 v105, v19
	v_mov_b32_e32 v106, v19
	v_mov_b32_e32 v107, v19
	v_mov_b32_e32 v108, v19
	v_mov_b32_e32 v109, v19
	v_mov_b32_e32 v110, v19
	v_mov_b32_e32 v111, v19
	v_mov_b32_e32 v112, v19
	v_mov_b32_e32 v113, v19
	v_mov_b32_e32 v46, v19
	v_mov_b32_e32 v47, v19
	v_mov_b32_e32 v48, v19
	v_mov_b32_e32 v49, v19
	v_mov_b32_e32 v30, v19
	v_mov_b32_e32 v31, v19
	v_mov_b32_e32 v32, v19
	v_mov_b32_e32 v33, v19
	v_mov_b32_e32 v38, v19
	v_mov_b32_e32 v39, v19
	v_mov_b32_e32 v40, v19
	v_mov_b32_e32 v41, v19
	v_mov_b32_e32 v34, v19
	v_mov_b32_e32 v35, v19
	v_mov_b32_e32 v36, v19
	v_mov_b32_e32 v37, v19
	s_mov_b32 s60, 0
	s_add_i32 s63, s49, 2
	s_mul_i32 s73, s63, 11
	s_lshr_b32 s73, s73, 5
	s_mul_i32 s73, s73, 31
	s_add_i32 s62, s63, s73
	s_mov_b32 s64, 0
	s_mov_b32 s66, 1
	s_mov_b32 s67, 0
	s_add_i32 s75, s49, 6
	s_lshl_b32 s68, s75, 15
	s_mov_b32 s69, 0
	v_lshl_add_u64 v[178:179], v[116:117], 0, s[68:69]
	s_add_i32 s70, s52, 0xc000
	v_lshl_add_u64 v[180:181], v[178:179], 0, s[34:35]
	v_mov_b32_e32 v174, v126
	v_mov_b32_e32 v202, 0x80000
	v_cmp_ne_u64_e64 s[76:77], v[184:185], s[30:31]
	s_nop 1
	v_cndmask_b32_e64 v196, 0, v202, s[76:77]
	v_cmp_ne_u64_e64 s[76:77], v[186:187], s[30:31]
	s_nop 1
	v_cndmask_b32_e64 v197, 0, v202, s[76:77]
	v_cmp_ne_u64_e64 s[76:77], v[188:189], s[30:31]
	s_nop 1
	v_cndmask_b32_e64 v198, 0, v202, s[76:77]
	v_cmp_ne_u64_e64 s[76:77], v[190:191], s[30:31]
	s_nop 1
	v_cndmask_b32_e64 v199, 0, v202, s[76:77]
	v_cmp_ne_u64_e64 s[76:77], v[192:193], s[30:31]
	s_nop 1
	v_cndmask_b32_e64 v200, 0, v202, s[76:77]
	v_cmp_ne_u64_e64 s[76:77], v[194:195], s[30:31]
	s_nop 1
	v_cndmask_b32_e64 v201, 0, v202, s[76:77]

.Lc4_bar:
	s_barrier
	s_waitcnt lgkmcnt(5)
	v_mfma_f32_16x16x32_f16 v[110:113], v[62:65], v[70:73], v[110:113]
	ds_read_b128 v[142:145], v174
	v_mfma_f32_16x16x32_f16 v[106:109], v[58:61], v[70:73], v[106:109]
	v_xor_b32_e32 v176, 64, v139
	s_waitcnt lgkmcnt(5)
	v_mfma_f32_16x16x32_f16 v[94:97], v[62:65], v[66:69], v[94:97]
	ds_read_b128 v[146:149], v174 offset:2048
	v_mfma_f32_16x16x32_f16 v[74:77], v[58:61], v[66:69], v[74:77]
	v_xor_b32_e32 v177, 64, v140
	s_mov_b32 m0, s70
	s_add_i32 s71, s38, 0x4000
	global_load_lds_dwordx4 v[178:179], off
	s_waitcnt lgkmcnt(5)
	v_mfma_f32_16x16x32_f16 v[42:45], v[62:65], v[82:85], v[42:45]
	ds_read_b128 v[150:153], v176
	v_mfma_f32_16x16x32_f16 v[26:29], v[58:61], v[82:85], v[26:29]
	s_and_b32 s71, s71, 0xc000
	s_add_i32 s72, s70, 0x400
	s_waitcnt lgkmcnt(5)
	v_mfma_f32_16x16x32_f16 v[46:49], v[62:65], v[78:81], v[46:49]
	ds_read_b128 v[154:157], v176 offset:2048
	v_mfma_f32_16x16x32_f16 v[30:33], v[58:61], v[78:81], v[30:33]
	v_add_u32_e32 v175, s71, v125
	s_waitcnt lgkmcnt(5)
	v_mfma_f32_16x16x32_f16 v[102:105], v[90:93], v[70:73], v[102:105]
	ds_read_b128 v[158:161], v177
	s_waitcnt lgkmcnt(5)
	v_mfma_f32_16x16x32_f16 v[98:101], v[86:89], v[70:73], v[98:101]
	v_mfma_f32_16x16x32_f16 v[54:57], v[90:93], v[66:69], v[54:57]
	ds_read_b128 v[162:165], v177 offset:2048
	v_mfma_f32_16x16x32_f16 v[50:53], v[86:89], v[66:69], v[50:53]
	v_add_u32_e32 v182, s62, v123
	v_mfma_f32_16x16x32_f16 v[22:25], v[90:93], v[82:85], v[22:25]
	ds_read_b128 v[166:169], v174 offset:4096
	v_mfma_f32_16x16x32_f16 v[18:21], v[86:89], v[82:85], v[18:21]
	v_bitop3_b32 v183, v182, v122, 6 bitop3:0x6c
	v_lshl_add_u32 v182, v182, 7, s64
	v_mfma_f32_16x16x32_f16 v[38:41], v[90:93], v[78:81], v[38:41]
	ds_read_b128 v[170:173], v174 offset:6144
	v_mfma_f32_16x16x32_f16 v[34:37], v[86:89], v[78:81], v[34:37]
	v_lshl_or_b32 v139, v183, 4, v182
	v_add_u32_e32 v174, s71, v126
	s_waitcnt lgkmcnt(5)
	v_mfma_f32_16x16x32_f16 v[110:113], v[142:145], v[150:153], v[110:113]
	ds_read_b128 v[62:65], v175
	v_mfma_f32_16x16x32_f16 v[106:109], v[146:149], v[150:153], v[106:109]
	s_mov_b32 m0, s72
	s_add_i32 s63, s63, 2
	global_load_lds_dwordx4 v[180:181], off
	s_waitcnt lgkmcnt(5)
	v_mfma_f32_16x16x32_f16 v[94:97], v[142:145], v[154:157], v[94:97]
	ds_read_b128 v[58:61], v175 offset:2048
	v_mfma_f32_16x16x32_f16 v[74:77], v[146:149], v[154:157], v[74:77]
	v_add_u32_e32 v182, s62, v124
	s_waitcnt lgkmcnt(5)
	v_mfma_f32_16x16x32_f16 v[42:45], v[142:145], v[158:161], v[42:45]
	ds_read_b128 v[70:73], v139
	v_mfma_f32_16x16x32_f16 v[26:29], v[146:149], v[158:161], v[26:29]
	v_bitop3_b32 v183, v182, v122, 6 bitop3:0x6c
	v_lshl_add_u32 v182, v182, 7, s64
	s_waitcnt lgkmcnt(5)
	v_mfma_f32_16x16x32_f16 v[46:49], v[142:145], v[162:165], v[46:49]
	ds_read_b128 v[66:69], v139 offset:2048
	v_mfma_f32_16x16x32_f16 v[30:33], v[146:149], v[162:165], v[30:33]
	v_lshl_or_b32 v140, v183, 4, v182
	s_waitcnt lgkmcnt(5)
	v_mfma_f32_16x16x32_f16 v[102:105], v[166:169], v[150:153], v[102:105]
	ds_read_b128 v[82:85], v140
	s_waitcnt lgkmcnt(5)
	v_mfma_f32_16x16x32_f16 v[98:101], v[170:173], v[150:153], v[98:101]
	s_cmp_ge_u32 s63, 9
	s_cselect_b32 s73, 9, 0
	s_cselect_b32 s74, 0xc000, 0
	s_sub_i32 s63, s63, s73
	s_xor_b32 s64, s64, s74
	v_mfma_f32_16x16x32_f16 v[54:57], v[166:169], v[154:157], v[54:57]
	ds_read_b128 v[78:81], v140 offset:2048
	s_mul_i32 s73, s63, 11
	s_lshr_b32 s73, s73, 5
	s_mul_i32 s73, s73, 31
	s_add_i32 s62, s63, s73
	v_mfma_f32_16x16x32_f16 v[50:53], v[170:173], v[154:157], v[50:53]
	s_addk_i32 s38, 0x4000
	s_add_i32 s60, s60, 1
	s_add_i32 s75, s60, 3
	s_cmp_lt_u32 s60, 33
	s_cselect_b32 s75, s75, 35
	s_lshl_b32 s75, s75, 1
	s_add_i32 s75, s75, s49
	s_lshl_b32 s68, s75, 15
	v_mfma_f32_16x16x32_f16 v[22:25], v[166:169], v[158:161], v[22:25]
	ds_read_b128 v[90:93], v175 offset:4096
	v_mfma_f32_16x16x32_f16 v[18:21], v[170:173], v[158:161], v[18:21]
	v_lshl_add_u64 v[178:179], v[116:117], 0, s[68:69]
	s_add_i32 s70, s38, 0xc000
	s_and_b32 s70, s70, 0xc000
	s_add_i32 s70, s70, s52
	v_mfma_f32_16x16x32_f16 v[38:41], v[166:169], v[162:165], v[38:41]
	ds_read_b128 v[86:89], v175 offset:6144
	v_lshl_add_u64 v[180:181], v[178:179], 0, s[34:35]
	v_mfma_f32_16x16x32_f16 v[34:37], v[170:173], v[162:165], v[34:37]
	s_cmp_lg_u32 s60, s66
	s_cbranch_scc1 .Lc4_nopatch
	s_bitcmp1_b32 s53, 0
	s_cselect_b32 s56, 0xc000, 0
	s_add_i32 m0, s56, s43
	v_mad_u64_u32 v[118:119], s[76:77], v196, s53, v[184:185]
	global_load_lds_dwordx4 v[118:119], off
	s_add_i32 m0, s56, s44
	v_mad_u64_u32 v[118:119], s[76:77], v197, s53, v[186:187]
	global_load_lds_dwordx4 v[118:119], off
	s_add_i32 m0, s56, s45
	v_mad_u64_u32 v[118:119], s[76:77], v198, s53, v[188:189]
	global_load_lds_dwordx4 v[118:119], off
	s_add_i32 m0, s56, s46
	v_mad_u64_u32 v[118:119], s[76:77], v199, s53, v[190:191]
	global_load_lds_dwordx4 v[118:119], off
	s_add_i32 m0, s56, s47
	v_mad_u64_u32 v[118:119], s[76:77], v200, s53, v[192:193]
	global_load_lds_dwordx4 v[118:119], off
	s_add_i32 m0, s56, s50
	v_mad_u64_u32 v[118:119], s[76:77], v201, s53, v[194:195]
	global_load_lds_dwordx4 v[118:119], off
	s_add_i32 s53, s53, 1
	s_mul_i32 s66, s53, 9
	s_add_i32 s66, s66, -8
	s_lshr_b32 s66, s66, 1
	s_add_i32 s66, s66, 1
	s_cmp_gt_u32 s53, 7
	s_cselect_b32 s66, 0x3e8, s66
	s_mov_b32 s67, 2

	.amdhsa_kernel _Z6conv_kILi512ELi256ELi3ELi64ELi1ELi1ELb0EEvPKDF16_S1_PKfS3_PDF16_S4_S1_fS3_S3_S3_S3_
		.amdhsa_group_segment_fixed_size 163840
		.amdhsa_private_segment_fixed_size 0
		.amdhsa_kernarg_size 96
		.amdhsa_user_sgpr_count 2
		.amdhsa_user_sgpr_dispatch_ptr 0
		.amdhsa_user_sgpr_queue_ptr 0
		.amdhsa_user_sgpr_kernarg_segment_ptr 1
		.amdhsa_user_sgpr_dispatch_id 0
		.amdhsa_user_sgpr_kernarg_preload_length 0
		.amdhsa_user_sgpr_kernarg_preload_offset 0
		.amdhsa_user_sgpr_private_segment_size 0
		.amdhsa_uses_dynamic_stack 0
		.amdhsa_enable_private_segment 0
		.amdhsa_system_sgpr_workgroup_id_x 1
		.amdhsa_system_sgpr_workgroup_id_y 0
		.amdhsa_system_sgpr_workgroup_id_z 0
		.amdhsa_system_sgpr_workgroup_info 0
		.amdhsa_system_vgpr_workitem_id 0
		.amdhsa_next_free_vgpr 204
		.amdhsa_next_free_sgpr 96
		.amdhsa_accum_offset 204
		.amdhsa_reserve_vcc 1
		.amdhsa_float_round_mode_32 0
		.amdhsa_float_round_mode_16_64 0
		.amdhsa_float_denorm_mode_32 3
		.amdhsa_float_denorm_mode_16_64 3
		.amdhsa_dx10_clamp 1
		.amdhsa_ieee_mode 1
		.amdhsa_fp16_overflow 0
		.amdhsa_tg_split 0
		.amdhsa_exception_fp_ieee_invalid_op 0
		.amdhsa_exception_fp_denorm_src 0
		.amdhsa_exception_fp_ieee_div_zero 0
		.amdhsa_exception_fp_ieee_overflow 0
		.amdhsa_exception_fp_ieee_underflow 0
		.amdhsa_exception_fp_ieee_inexact 0
		.amdhsa_exception_int_div_zero 0
	.end_amdhsa_kernel

amdhsa.kernels:
  - .agpr_count:     0
    .args:
      - .actual_access:  read_only
        .address_space:  global
        .offset:         0
        .size:           8
        .value_kind:     global_buffer
      - .actual_access:  read_only
        .address_space:  global
        .offset:         8
        .size:           8
        .value_kind:     global_buffer
      - .actual_access:  read_only
        .address_space:  global
        .offset:         16
        .size:           8
        .value_kind:     global_buffer
      - .actual_access:  read_only
        .address_space:  global
        .offset:         24
        .size:           8
        .value_kind:     global_buffer
      - .actual_access:  read_only
        .address_space:  global
        .offset:         32
        .size:           8
        .value_kind:     global_buffer
      - .actual_access:  read_only
        .address_space:  global
        .offset:         40
        .size:           8
        .value_kind:     global_buffer
      - .actual_access:  write_only
        .address_space:  global
        .offset:         48
        .size:           8
        .value_kind:     global_buffer
      - .actual_access:  write_only
        .address_space:  global
        .offset:         56
        .size:           8
        .value_kind:     global_buffer
      - .actual_access:  write_only
        .address_space:  global
        .offset:         64
        .size:           8
        .value_kind:     global_buffer
      - .actual_access:  write_only
        .address_space:  global
        .offset:         72
        .size:           8
        .value_kind:     global_buffer
      - .actual_access:  write_only
        .address_space:  global
        .offset:         80
        .size:           8
        .value_kind:     global_buffer
      - .actual_access:  write_only
        .address_space:  global
        .offset:         88
        .size:           8
        .value_kind:     global_buffer
      - .actual_access:  read_only
        .address_space:  global
        .offset:         96
        .size:           8
        .value_kind:     global_buffer
      - .actual_access:  read_only
        .address_space:  global
        .offset:         104
        .size:           8
        .value_kind:     global_buffer
      - .actual_access:  read_only
        .address_space:  global
        .offset:         112
        .size:           8
        .value_kind:     global_buffer
      - .actual_access:  read_only
        .address_space:  global
        .offset:         120
        .size:           8
        .value_kind:     global_buffer
      - .actual_access:  write_only
        .address_space:  global
        .offset:         128
        .size:           8
        .value_kind:     global_buffer
      - .actual_access:  write_only
        .address_space:  global
        .offset:         136
        .size:           8
        .value_kind:     global_buffer
    .group_segment_fixed_size: 14400
    .kernarg_segment_align: 8
    .kernarg_segment_size: 144
    .language:       OpenCL C
    .language_version:
      - 2
      - 0
    .max_flat_workgroup_size: 256
    .name:           _Z10prep_all_kPKfS0_S0_S0_S0_S0_PDF16_S1_S1_S1_S1_S1_S0_S0_S0_S0_S1_Pj
    .private_segment_fixed_size: 0
    .sgpr_count:     27
    .sgpr_spill_count: 0
    .symbol:         _Z10prep_all_kPKfS0_S0_S0_S0_S0_PDF16_S1_S1_S1_S1_S1_S0_S0_S0_S0_S1_Pj.kd
    .uniform_work_group_size: 1
    .uses_dynamic_stack: false
    .vgpr_count:     64
    .vgpr_spill_count: 0
    .wavefront_size: 64
  - .agpr_count:     0
    .args:
      - .actual_access:  read_only
        .address_space:  global
        .offset:         0
        .size:           8
        .value_kind:     global_buffer
      - .actual_access:  read_only
        .address_space:  global
        .offset:         8
        .size:           8
        .value_kind:     global_buffer
      - .actual_access:  read_only
        .address_space:  global
        .offset:         16
        .size:           8
        .value_kind:     global_buffer
      - .actual_access:  read_only
        .address_space:  global
        .offset:         24
        .size:           8
        .value_kind:     global_buffer
      - .actual_access:  read_only
        .address_space:  global
        .offset:         32
        .size:           8
        .value_kind:     global_buffer
      - .actual_access:  read_only
        .address_space:  global
        .offset:         40
        .size:           8
        .value_kind:     global_buffer
      - .actual_access:  write_only
        .address_space:  global
        .offset:         48
        .size:           8
        .value_kind:     global_buffer
    .group_segment_fixed_size: 0
    .kernarg_segment_align: 8
    .kernarg_segment_size: 56
    .language:       OpenCL C
    .language_version:
      - 2
      - 0
    .max_flat_workgroup_size: 256
    .name:           _Z9finish6_kPKDF16_PKfS2_S2_S2_S2_Pf
    .private_segment_fixed_size: 0
    .sgpr_count:     18
    .sgpr_spill_count: 0
    .symbol:         _Z9finish6_kPKDF16_PKfS2_S2_S2_S2_Pf.kd
    .uniform_work_group_size: 1
    .uses_dynamic_stack: false
    .vgpr_count:     51
    .vgpr_spill_count: 0
    .wavefront_size: 64
  - .agpr_count:     0
    .args:
      - .actual_access:  read_only
        .address_space:  global
        .offset:         0
        .size:           8
        .value_kind:     global_buffer
      - .actual_access:  write_only
        .address_space:  global
        .offset:         8
        .size:           8
        .value_kind:     global_buffer
    .group_segment_fixed_size: 16640
    .kernarg_segment_align: 8
    .kernarg_segment_size: 16
    .language:       OpenCL C
    .language_version:
      - 2
      - 0
    .max_flat_workgroup_size: 256
    .name:           _Z6gram_kPKfPf
    .private_segment_fixed_size: 0
    .sgpr_count:     16
    .sgpr_spill_count: 0
    .symbol:         _Z6gram_kPKfPf.kd
    .uniform_work_group_size: 1
    .uses_dynamic_stack: false
    .vgpr_count:     38
    .vgpr_spill_count: 0
    .wavefront_size: 64
  - .agpr_count:     0
    .args:
      - .actual_access:  read_only
        .address_space:  global
        .offset:         0
        .size:           8
        .value_kind:     global_buffer
      - .address_space:  global
        .offset:         8
        .size:           8
        .value_kind:     global_buffer
      - .actual_access:  read_only
        .address_space:  global
        .offset:         16
        .size:           8
        .value_kind:     global_buffer
      - .actual_access:  read_only
        .address_space:  global
        .offset:         24
        .size:           8
        .value_kind:     global_buffer
      - .actual_access:  read_only
        .address_space:  global
        .offset:         32
        .size:           8
        .value_kind:     global_buffer
      - .actual_access:  write_only
        .address_space:  global
        .offset:         40
        .size:           8
        .value_kind:     global_buffer
      - .actual_access:  read_only
        .address_space:  global
        .offset:         48
        .size:           8
        .value_kind:     global_buffer
      - .offset:         56
        .size:           4
        .value_kind:     by_value
      - .actual_access:  read_only
        .address_space:  global
        .offset:         64
        .size:           8
        .value_kind:     global_buffer
      - .actual_access:  read_only
        .address_space:  global
        .offset:         72
        .size:           8
        .value_kind:     global_buffer
      - .actual_access:  read_only
        .address_space:  global
        .offset:         80
        .size:           8
        .value_kind:     global_buffer
      - .actual_access:  read_only
        .address_space:  global
        .offset:         88
        .size:           8
        .value_kind:     global_buffer
    .group_segment_fixed_size: 147456
    .kernarg_segment_align: 8
    .kernarg_segment_size: 96
    .language:       OpenCL C
    .language_version:
      - 2
      - 0
    .max_flat_workgroup_size: 512
    .name:           _Z6conv_kILi64ELi128ELi20ELi128ELi4ELi4ELb1EEvPKDF16_S1_PKfS3_PDF16_S4_S1_fS3_S3_S3_S3_
    .private_segment_fixed_size: 0
    .sgpr_count:     43
    .sgpr_spill_count: 0
    .symbol:         _Z6conv_kILi64ELi128ELi20ELi128ELi4ELi4ELb1EEvPKDF16_S1_PKfS3_PDF16_S4_S1_fS3_S3_S3_S3_.kd
    .uniform_work_group_size: 1
    .uses_dynamic_stack: false
    .vgpr_count:     160
    .vgpr_spill_count: 0
    .wavefront_size: 64
  - .agpr_count:     0
    .args:
      - .actual_access:  read_only
        .address_space:  global
        .offset:         0
        .size:           8
        .value_kind:     global_buffer
      - .actual_access:  read_only
        .address_space:  global
        .offset:         8
        .size:           8
        .value_kind:     global_buffer
      - .actual_access:  read_only
        .address_space:  global
        .offset:         16
        .size:           8
        .value_kind:     global_buffer
      - .actual_access:  write_only
        .address_space:  global
        .offset:         24
        .size:           8
        .value_kind:     global_buffer
    .group_segment_fixed_size: 0
    .kernarg_segment_align: 8
    .kernarg_segment_size: 32
    .language:       OpenCL C
    .language_version:
      - 2
      - 0
    .max_flat_workgroup_size: 256
    .name:           _Z8finish_kILi128ELi4EEvPKDF16_PKfS3_PDF16_
    .private_segment_fixed_size: 0
    .sgpr_count:     18
    .sgpr_spill_count: 0
    .symbol:         _Z8finish_kILi128ELi4EEvPKDF16_PKfS3_PDF16_.kd
    .uniform_work_group_size: 1
    .uses_dynamic_stack: false
    .vgpr_count:     44
    .vgpr_spill_count: 0
    .wavefront_size: 64
  - .agpr_count:     0
    .args:
      - .address_space:  global
        .offset:         0
        .size:           8
        .value_kind:     global_buffer
      - .address_space:  global
        .offset:         8
        .size:           8
        .value_kind:     global_buffer
      - .address_space:  global
        .offset:         16
        .size:           8
        .value_kind:     global_buffer
      - .actual_access:  read_only
        .address_space:  global
        .offset:         24
        .size:           8
        .value_kind:     global_buffer
      - .actual_access:  write_only
        .address_space:  global
        .offset:         32
        .size:           8
        .value_kind:     global_buffer
      - .actual_access:  read_only
        .address_space:  global
        .offset:         40
        .size:           8
        .value_kind:     global_buffer
      - .address_space:  global
        .offset:         48
        .size:           8
        .value_kind:     global_buffer
      - .offset:         56
        .size:           4
        .value_kind:     by_value
      - .actual_access:  read_only
        .address_space:  global
        .offset:         64
        .size:           8
        .value_kind:     global_buffer
      - .actual_access:  read_only
        .address_space:  global
        .offset:         72
        .size:           8
        .value_kind:     global_buffer
      - .actual_access:  read_only
        .address_space:  global
        .offset:         80
        .size:           8
        .value_kind:     global_buffer
      - .actual_access:  read_only
        .address_space:  global
        .offset:         88
        .size:           8
        .value_kind:     global_buffer
    .group_segment_fixed_size: 163840
    .kernarg_segment_align: 8
    .kernarg_segment_size: 96
    .language:       OpenCL C
    .language_version:
      - 2
      - 0
    .max_flat_workgroup_size: 512
    .name:           _Z6conv_kILi128ELi256ELi3ELi64ELi1ELi1ELb0EEvPKDF16_S1_PKfS3_PDF16_S4_S1_fS3_S3_S3_S3_
    .private_segment_fixed_size: 0
    .sgpr_count:     51
    .sgpr_spill_count: 0
    .symbol:         _Z6conv_kILi128ELi256ELi3ELi64ELi1ELi1ELb0EEvPKDF16_S1_PKfS3_PDF16_S4_S1_fS3_S3_S3_S3_.kd
    .uniform_work_group_size: 1
    .uses_dynamic_stack: false
    .vgpr_count:     184
    .vgpr_spill_count: 0
    .wavefront_size: 64
  - .agpr_count:     0
    .args:
      - .address_space:  global
        .offset:         0
        .size:           8
        .value_kind:     global_buffer
      - .address_space:  global
        .offset:         8
        .size:           8
        .value_kind:     global_buffer
      - .address_space:  global
        .offset:         16
        .size:           8
        .value_kind:     global_buffer
      - .actual_access:  read_only
        .address_space:  global
        .offset:         24
        .size:           8
        .value_kind:     global_buffer
      - .actual_access:  write_only
        .address_space:  global
        .offset:         32
        .size:           8
        .value_kind:     global_buffer
      - .actual_access:  read_only
        .address_space:  global
        .offset:         40
        .size:           8
        .value_kind:     global_buffer
      - .address_space:  global
        .offset:         48
        .size:           8
        .value_kind:     global_buffer
      - .offset:         56
        .size:           4
        .value_kind:     by_value
      - .actual_access:  read_only
        .address_space:  global
        .offset:         64
        .size:           8
        .value_kind:     global_buffer
      - .actual_access:  read_only
        .address_space:  global
        .offset:         72
        .size:           8
        .value_kind:     global_buffer
      - .actual_access:  read_only
        .address_space:  global
        .offset:         80
        .size:           8
        .value_kind:     global_buffer
      - .actual_access:  read_only
        .address_space:  global
        .offset:         88
        .size:           8
        .value_kind:     global_buffer
    .group_segment_fixed_size: 163840
    .kernarg_segment_align: 8
    .kernarg_segment_size: 96
    .language:       OpenCL C
    .language_version:
      - 2
      - 0
    .max_flat_workgroup_size: 512
    .name:           _Z6conv_kILi256ELi512ELi3ELi128ELi1ELi1ELb0EEvPKDF16_S1_PKfS3_PDF16_S4_S1_fS3_S3_S3_S3_
    .private_segment_fixed_size: 0
    .sgpr_count:     64
    .sgpr_spill_count: 0
    .symbol:         _Z6conv_kILi256ELi512ELi3ELi128ELi1ELi1ELb0EEvPKDF16_S1_PKfS3_PDF16_S4_S1_fS3_S3_S3_S3_.kd
    .uniform_work_group_size: 1
    .uses_dynamic_stack: false
    .vgpr_count:     184
    .vgpr_spill_count: 0
    .wavefront_size: 64
  - .agpr_count:     0
    .args:
      - .address_space:  global
        .offset:         0
        .size:           8
        .value_kind:     global_buffer
      - .address_space:  global
        .offset:         8
        .size:           8
        .value_kind:     global_buffer
      - .address_space:  global
        .offset:         16
        .size:           8
        .value_kind:     global_buffer
      - .actual_access:  read_only
        .address_space:  global
        .offset:         24
        .size:           8
        .value_kind:     global_buffer
      - .actual_access:  write_only
        .address_space:  global
        .offset:         32
        .size:           8
        .value_kind:     global_buffer
      - .actual_access:  read_only
        .address_space:  global
        .offset:         40
        .size:           8
        .value_kind:     global_buffer
      - .address_space:  global
        .offset:         48
        .size:           8
        .value_kind:     global_buffer
      - .offset:         56
        .size:           4
        .value_kind:     by_value
      - .actual_access:  read_only
        .address_space:  global
        .offset:         64
        .size:           8
        .value_kind:     global_buffer
      - .actual_access:  read_only
        .address_space:  global
        .offset:         72
        .size:           8
        .value_kind:     global_buffer
      - .actual_access:  read_only
        .address_space:  global
        .offset:         80
        .size:           8
        .value_kind:     global_buffer
      - .actual_access:  read_only
        .address_space:  global
        .offset:         88
        .size:           8
        .value_kind:     global_buffer
    .group_segment_fixed_size: 163840
    .kernarg_segment_align: 8
    .kernarg_segment_size: 96
    .language:       OpenCL C
    .language_version:
      - 2
      - 0
    .max_flat_workgroup_size: 512
    .name:           _Z6conv_kILi512ELi256ELi3ELi64ELi1ELi1ELb0EEvPKDF16_S1_PKfS3_PDF16_S4_S1_fS3_S3_S3_S3_
    .private_segment_fixed_size: 0
    .sgpr_count:     66
    .sgpr_spill_count: 0
    .symbol:         _Z6conv_kILi512ELi256ELi3ELi64ELi1ELi1ELb0EEvPKDF16_S1_PKfS3_PDF16_S4_S1_fS3_S3_S3_S3_.kd
    .uniform_work_group_size: 1
    .uses_dynamic_stack: false
    .vgpr_count:     204
    .vgpr_spill_count: 0
    .wavefront_size: 64
  - .agpr_count:     0
    .args:
      - .address_space:  global
        .offset:         0
        .size:           8
        .value_kind:     global_buffer
      - .address_space:  global
        .offset:         8
        .size:           8
        .value_kind:     global_buffer
      - .actual_access:  read_only
        .address_space:  global
        .offset:         16
        .size:           8
        .value_kind:     global_buffer
      - .actual_access:  read_only
        .address_space:  global
        .offset:         24
        .size:           8
        .value_kind:     global_buffer
      - .actual_access:  read_only
        .address_space:  global
        .offset:         32
        .size:           8
        .value_kind:     global_buffer
      - .actual_access:  write_only
        .address_space:  global
        .offset:         40
        .size:           8
        .value_kind:     global_buffer
      - .address_space:  global
        .offset:         48
        .size:           8
        .value_kind:     global_buffer
      - .offset:         56
        .size:           4
        .value_kind:     by_value
      - .actual_access:  read_only
        .address_space:  global
        .offset:         64
        .size:           8
        .value_kind:     global_buffer
      - .actual_access:  read_only
        .address_space:  global
        .offset:         72
        .size:           8
        .value_kind:     global_buffer
      - .actual_access:  read_only
        .address_space:  global
        .offset:         80
        .size:           8
        .value_kind:     global_buffer
      - .actual_access:  read_only
        .address_space:  global
        .offset:         88
        .size:           8
        .value_kind:     global_buffer
    .group_segment_fixed_size: 163840
    .kernarg_segment_align: 8
    .kernarg_segment_size: 96
    .language:       OpenCL C
    .language_version:
      - 2
      - 0
    .max_flat_workgroup_size: 512
    .name:           _Z6conv_kILi256ELi128ELi3ELi64ELi1ELi2ELb0EEvPKDF16_S1_PKfS3_PDF16_S4_S1_fS3_S3_S3_S3_
    .private_segment_fixed_size: 0
    .sgpr_count:     55
    .sgpr_spill_count: 0
    .symbol:         _Z6conv_kILi256ELi128ELi3ELi64ELi1ELi2ELb0EEvPKDF16_S1_PKfS3_PDF16_S4_S1_fS3_S3_S3_S3_.kd
    .uniform_work_group_size: 1
    .uses_dynamic_stack: false
    .vgpr_count:     172
    .vgpr_spill_count: 0
    .wavefront_size: 64
  - .agpr_count:     0
    .args:
      - .actual_access:  read_only
        .address_space:  global
        .offset:         0
        .size:           8
        .value_kind:     global_buffer
      - .actual_access:  read_only
        .address_space:  global
        .offset:         8
        .size:           8
        .value_kind:     global_buffer
      - .actual_access:  read_only
        .address_space:  global
        .offset:         16
        .size:           8
        .value_kind:     global_buffer
      - .actual_access:  write_only
        .address_space:  global
        .offset:         24
        .size:           8
        .value_kind:     global_buffer
    .group_segment_fixed_size: 0
    .kernarg_segment_align: 8
    .kernarg_segment_size: 32
    .language:       OpenCL C
    .language_version:
      - 2
      - 0
    .max_flat_workgroup_size: 256
    .name:           _Z8finish_kILi128ELi2EEvPKDF16_PKfS3_PDF16_
    .private_segment_fixed_size: 0
    .sgpr_count:     18
    .sgpr_spill_count: 0
    .symbol:         _Z8finish_kILi128ELi2EEvPKDF16_PKfS3_PDF16_.kd
    .uniform_work_group_size: 1
    .uses_dynamic_stack: false
    .vgpr_count:     28
    .vgpr_spill_count: 0
    .wavefront_size: 64
  - .agpr_count:     0
    .args:
      - .address_space:  global
        .offset:         0
        .size:           8
        .value_kind:     global_buffer
      - .address_space:  global
        .offset:         8
        .size:           8
        .value_kind:     global_buffer
      - .actual_access:  read_only
        .address_space:  global
        .offset:         16
        .size:           8
        .value_kind:     global_buffer
      - .actual_access:  read_only
        .address_space:  global
        .offset:         24
        .size:           8
        .value_kind:     global_buffer
      - .actual_access:  read_only
        .address_space:  global
        .offset:         32
        .size:           8
        .value_kind:     global_buffer
      - .actual_access:  write_only
        .address_space:  global
        .offset:         40
        .size:           8
        .value_kind:     global_buffer
      - .address_space:  global
        .offset:         48
        .size:           8
        .value_kind:     global_buffer
      - .offset:         56
        .size:           4
        .value_kind:     by_value
      - .actual_access:  read_only
        .address_space:  global
        .offset:         64
        .size:           8
        .value_kind:     global_buffer
      - .actual_access:  read_only
        .address_space:  global
        .offset:         72
        .size:           8
        .value_kind:     global_buffer
      - .actual_access:  read_only
        .address_space:  global
        .offset:         80
        .size:           8
        .value_kind:     global_buffer
      - .actual_access:  read_only
        .address_space:  global
        .offset:         88
        .size:           8
        .value_kind:     global_buffer
    .group_segment_fixed_size: 147456
    .kernarg_segment_align: 8
    .kernarg_segment_size: 96
    .language:       OpenCL C
    .language_version:
      - 2
      - 0
    .max_flat_workgroup_size: 512
    .name:           _Z6conv_kILi128ELi64ELi20ELi64ELi4ELi4ELb0EEvPKDF16_S1_PKfS3_PDF16_S4_S1_fS3_S3_S3_S3_
    .private_segment_fixed_size: 0
    .sgpr_count:     64
    .sgpr_spill_count: 0
    .symbol:         _Z6conv_kILi128ELi64ELi20ELi64ELi4ELi4ELb0EEvPKDF16_S1_PKfS3_PDF16_S4_S1_fS3_S3_S3_S3_.kd
    .uniform_work_group_size: 1
    .uses_dynamic_stack: false
    .vgpr_count:     184
    .vgpr_spill_count: 0
    .wavefront_size: 64
